# speedup vs baseline: 1.0325x; 1.0113x over previous
_Z9k_gemm_tlILi2ELb1EEvPKDF16_6TlArgs:
	s_load_dwordx4 s[12:15], s[0:1], 0x0
	s_load_dwordx8 s[4:11], s[0:1], 0x18
	v_lshrrev_b32_e32 v99, 6, v0
	s_lshr_b32 s16, s2, 6
	s_lshl_b32 s2, s2, 6
	s_mov_b32 s17, 0
	s_and_b32 s2, s2, 0xfc0
	v_lshl_or_b32 v86, s3, 2, v99
	v_mov_b32_e32 v87, 0
	s_lshl_b64 s[18:19], s[16:17], 21
	v_lshlrev_b64 v[2:3], 15, v[86:87]
	s_or_b32 s18, s18, s2
	s_waitcnt lgkmcnt(0)
	s_lshl_b32 s21, s3, 7
	v_lshrrev_b32_e32 v140, 4, v0
	v_or_b32_e32 v140, s21, v140
	v_lshlrev_b32_e32 v140, 2, v140
	global_load_dword v124, v140, s[10:11]
	global_load_dword v126, v140, s[10:11] offset:64
	global_load_dword v128, v140, s[10:11] offset:128
	global_load_dword v130, v140, s[10:11] offset:192
	global_load_dword v132, v140, s[10:11] offset:256
	global_load_dword v134, v140, s[10:11] offset:320
	global_load_dword v136, v140, s[10:11] offset:384
	global_load_dword v138, v140, s[10:11] offset:448
	v_lshl_add_u64 v[2:3], s[12:13], 0, v[2:3]
	v_lshlrev_b32_e32 v1, 4, v0
	s_lshl_b64 s[12:13], s[18:19], 1
	v_and_b32_e32 v86, 0x3f0, v1
	s_add_u32 s12, s14, s12
	v_lshl_add_u64 v[88:89], v[2:3], 0, v[86:87]
	v_lshrrev_b32_e32 v100, 3, v0
	s_addc_u32 s13, s15, s13
	v_and_b32_e32 v86, 0x70, v1
	v_or_b32_e32 v98, 0x100, v0
	v_lshl_add_u64 v[2:3], s[12:13], 0, v[86:87]
	v_lshrrev_b32_e32 v101, 3, v98
	v_lshlrev_b32_e32 v86, 13, v100
	v_lshl_add_u64 v[92:93], v[2:3], 0, v[86:87]
	v_lshlrev_b32_e32 v86, 13, v101
	v_or_b32_e32 v107, 64, v100
	v_lshl_add_u64 v[90:91], v[2:3], 0, v[86:87]
	v_lshlrev_b32_e32 v86, 13, v107
	v_or_b32_e32 v106, 64, v101
	v_lshl_add_u64 v[6:7], v[2:3], 0, v[86:87]
	v_lshlrev_b32_e32 v86, 13, v106
	v_lshl_add_u64 v[8:9], v[2:3], 0, v[86:87]
	v_lshlrev_b32_e32 v86, 2, v0
	s_movk_i32 s20, 0x1000
	v_lshl_add_u64 v[2:3], s[4:5], 0, v[86:87]
	v_add_co_u32_e32 v4, vcc, s20, v2
	s_movk_i32 s12, 0x2000
	s_nop 0
	v_addc_co_u32_e32 v5, vcc, 0, v3, vcc
	v_add_co_u32_e32 v18, vcc, s12, v2
	s_movk_i32 s12, 0x3000
	s_nop 0
	v_addc_co_u32_e32 v19, vcc, 0, v3, vcc
	v_add_co_u32_e32 v20, vcc, s12, v2
	s_movk_i32 s12, 0x4000
	s_nop 0
	v_addc_co_u32_e32 v21, vcc, 0, v3, vcc
	v_add_co_u32_e32 v48, vcc, s12, v2
	s_movk_i32 s12, 0x5000
	s_nop 0
	v_addc_co_u32_e32 v49, vcc, 0, v3, vcc
	v_add_co_u32_e32 v50, vcc, s12, v2
	s_movk_i32 s12, 0x6000
	s_nop 0
	v_addc_co_u32_e32 v51, vcc, 0, v3, vcc
	v_add_co_u32_e32 v52, vcc, s12, v2
	s_movk_i32 s12, 0x7000
	s_nop 0
	v_addc_co_u32_e32 v53, vcc, 0, v3, vcc
	v_add_co_u32_e32 v54, vcc, s12, v2
	s_mov_b32 s12, 0x8000
	s_nop 0
	v_addc_co_u32_e32 v55, vcc, 0, v3, vcc
	global_load_dword v11, v86, s[4:5]
	global_load_dword v10, v86, s[4:5] offset:2048
	v_or_b32_e32 v1, 0x400, v0
	v_add_co_u32_e32 v56, vcc, s12, v2
	v_lshlrev_b32_e32 v15, 2, v1
	s_nop 0
	v_addc_co_u32_e32 v57, vcc, 0, v3, vcc
	s_mov_b32 s12, 0x9000
	global_load_dword v13, v15, s[4:5]
	global_load_dword v12, v[4:5], off offset:2048
	global_load_dword v14, v[18:19], off offset:2048
	v_add_co_u32_e32 v58, vcc, s12, v2
	s_mov_b32 s12, 0xa000
	s_nop 0
	v_addc_co_u32_e32 v59, vcc, 0, v3, vcc
	v_add_co_u32_e32 v60, vcc, s12, v2
	global_load_dword v15, v[20:21], off offset:-4096
	global_load_dword v17, v[20:21], off
	global_load_dword v16, v[20:21], off offset:2048
	global_load_dword v23, v[50:51], off offset:-4096
	global_load_dword v25, v[50:51], off
	v_addc_co_u32_e32 v61, vcc, 0, v3, vcc
	s_mov_b32 s12, 0xb000
	global_load_dword v24, v[50:51], off offset:2048
	global_load_dword v27, v[54:55], off offset:-4096
	global_load_dword v29, v[54:55], off
	global_load_dword v28, v[54:55], off offset:2048
	global_load_dword v22, v[48:49], off offset:2048
	global_load_dword v26, v[52:53], off offset:2048
	global_load_dword v30, v[56:57], off offset:2048
	v_add_co_u32_e32 v62, vcc, s12, v2
	s_mov_b32 s12, 0xc000
	s_nop 0
	v_addc_co_u32_e32 v63, vcc, 0, v3, vcc
	v_add_co_u32_e32 v64, vcc, s12, v2
	s_mov_b32 s12, 0xd000
	s_nop 0
	v_addc_co_u32_e32 v65, vcc, 0, v3, vcc
	v_add_co_u32_e32 v66, vcc, s12, v2
	global_load_dword v32, v[60:61], off offset:2048
	global_load_dword v31, v[58:59], off offset:-4096
	global_load_dword v35, v[58:59], off
	global_load_dword v34, v[58:59], off offset:2048
	global_load_dword v33, v[62:63], off offset:-4096
	global_load_dword v37, v[62:63], off
	v_addc_co_u32_e32 v67, vcc, 0, v3, vcc
	s_mov_b32 s12, 0xe000
	v_add_co_u32_e32 v46, vcc, s12, v2
	s_mov_b32 s12, 0xf000
	s_nop 0
	v_addc_co_u32_e32 v47, vcc, 0, v3, vcc
	v_add_co_u32_e32 v68, vcc, s12, v2
	s_load_dwordx4 s[12:15], s[0:1], 0x40
	s_nop 0
	v_addc_co_u32_e32 v69, vcc, 0, v3, vcc
	global_load_dword v36, v[62:63], off offset:2048
	global_load_dword v41, v[66:67], off offset:-4096
	global_load_dword v39, v[66:67], off
	global_load_dword v38, v[66:67], off offset:2048
	global_load_dword v43, v[68:69], off offset:-4096
	global_load_dword v40, v[64:65], off offset:2048
	global_load_dword v42, v[46:47], off offset:2048
	global_load_dword v45, v[68:69], off
	global_load_dword v44, v[68:69], off offset:2048
	global_load_dword v120, v86, s[6:7]
	global_load_dword v75, v86, s[4:5] offset:1024
	global_load_dword v76, v[20:21], off offset:3072
	global_load_dword v77, v[20:21], off offset:1024
	global_load_dword v74, v86, s[4:5] offset:3072
	global_load_dword v78, v[4:5], off offset:3072
	global_load_dword v80, v[18:19], off offset:3072
	global_load_dword v83, v[48:49], off offset:1024
	global_load_dword v81, v[18:19], off offset:1024
	global_load_dword v79, v[4:5], off offset:1024
	global_load_dword v84, v[54:55], off offset:3072
	global_load_dword v85, v[54:55], off offset:1024
	global_load_dword v94, v[50:51], off offset:3072
	global_load_dword v95, v[50:51], off offset:1024
	global_load_dword v82, v[48:49], off offset:3072
	global_load_dword v96, v[52:53], off offset:3072
	global_load_dword v102, v[56:57], off offset:3072
	global_load_dword v103, v[56:57], off offset:1024
	global_load_dword v97, v[52:53], off offset:1024
	global_load_dword v105, v[62:63], off offset:1024
	global_load_dword v108, v[58:59], off offset:3072
	global_load_dword v109, v[58:59], off offset:1024
	global_load_dword v110, v[60:61], off offset:3072
	global_load_dword v112, v[64:65], off offset:3072
	global_load_dword v115, v[46:47], off offset:1024
	global_load_dword v113, v[64:65], off offset:1024
	global_load_dword v111, v[60:61], off offset:1024
	global_load_dword v116, v[66:67], off offset:3072
	global_load_dword v117, v[66:67], off offset:1024
	global_load_dword v104, v[62:63], off offset:3072
	global_load_dword v121, v86, s[8:9]
	global_load_dword v122, v86, s[6:7] offset:1024
	global_load_dword v123, v86, s[8:9] offset:1024
	global_load_dword v114, v[46:47], off offset:3072
	global_load_dword v118, v[68:69], off offset:3072
	global_load_dword v119, v[68:69], off offset:1024
	global_load_dwordx4 v[18:21], v[88:89], off
	global_load_dwordx4 v[62:65], v[88:89], off offset:1024
	global_load_dwordx4 v[54:57], v[88:89], off offset:2048
	global_load_dwordx4 v[50:53], v[88:89], off offset:3072
	global_load_dwordx4 v[70:73], v[92:93], off
	global_load_dwordx4 v[2:5], v[90:91], off
	s_mov_b32 s4, 0x39000000
	s_cmp_eq_u32 s3, 0
	s_waitcnt vmcnt(62)
	v_pk_add_f32 v[10:11], v[10:11], 0 op_sel_hi:[1,0]
	s_nop 0
	v_pk_add_f32 v[10:11], v[10:11], v[12:13]
	s_nop 0
	v_pk_add_f32 v[10:11], v[10:11], v[14:15]
	s_nop 0
	v_pk_add_f32 v[10:11], v[10:11], v[16:17]
	s_waitcnt vmcnt(59)
	v_pk_add_f32 v[10:11], v[10:11], v[22:23]
	s_nop 0
	v_pk_add_f32 v[10:11], v[10:11], v[24:25]
	s_waitcnt vmcnt(1)
	v_cvt_f32_f16_e32 v22, v72
	v_pk_add_f32 v[10:11], v[10:11], v[26:27]
	v_cvt_f32_f16_sdwa v23, v72 dst_sel:DWORD dst_unused:UNUSED_PAD src0_sel:WORD_1
	v_pk_add_f32 v[10:11], v[10:11], v[28:29]
	v_cvt_f32_f16_e32 v24, v73
	v_pk_add_f32 v[10:11], v[10:11], v[30:31]
	v_cvt_f32_f16_sdwa v25, v73 dst_sel:DWORD dst_unused:UNUSED_PAD src0_sel:WORD_1
	v_pk_add_f32 v[10:11], v[10:11], v[34:35]
	s_nop 0
	v_pk_add_f32 v[10:11], v[10:11], v[32:33]
	s_nop 0
	v_pk_add_f32 v[10:11], v[10:11], v[36:37]
	s_nop 0
	v_pk_add_f32 v[10:11], v[10:11], v[40:41]
	s_nop 0
	v_pk_add_f32 v[10:11], v[10:11], v[38:39]
	s_nop 0
	v_pk_add_f32 v[10:11], v[10:11], v[42:43]
	s_nop 0
	v_pk_add_f32 v[10:11], v[10:11], v[44:45]
	s_nop 0
	v_pk_mul_f32 v[10:11], v[10:11], s[4:5] op_sel_hi:[1,0]
	s_mov_b32 s5, 0xf800000
	v_fma_f32 v10, -v11, v11, v10
	v_cmp_ngt_f32_e32 vcc, 0, v10
	s_nop 1
	v_cndmask_b32_e32 v10, 0, v10, vcc
	v_add_f32_e32 v10, 0x3727c5ac, v10
	v_mul_f32_e32 v12, 0x4f800000, v10
	v_cmp_gt_f32_e32 vcc, s5, v10
	s_nop 1
	v_cndmask_b32_e32 v10, v10, v12, vcc
	v_add_co_u32_e64 v12, s[0:1], s20, v88
	v_sqrt_f32_e32 v14, v10
	s_nop 0
	v_addc_co_u32_e64 v13, s[0:1], 0, v89, s[0:1]
	global_load_dwordx4 v[46:49], v[12:13], off
	global_load_dwordx4 v[38:41], v[12:13], off offset:1024
	global_load_dwordx4 v[42:45], v[12:13], off offset:2048
	global_load_dwordx4 v[34:37], v[12:13], off offset:3072
	global_load_dwordx4 v[66:69], v[6:7], off
	global_load_dwordx4 v[58:61], v[8:9], off
	v_add_u32_e32 v15, -1, v14
	v_fma_f32 v16, -v15, v14, v10
	v_cmp_ge_f32_e64 s[0:1], 0, v16
	v_add_u32_e32 v16, 1, v14
	s_nop 0
	v_cndmask_b32_e64 v15, v14, v15, s[0:1]
	v_fma_f32 v14, -v16, v14, v10
	v_cmp_lt_f32_e64 s[0:1], 0, v14
	s_nop 1
	v_cndmask_b32_e64 v14, v15, v16, s[0:1]
	v_mul_f32_e32 v15, 0x37800000, v14
	v_cndmask_b32_e32 v14, v14, v15, vcc
	v_mov_b32_e32 v15, 0x260
	v_cmp_class_f32_e32 vcc, v10, v15
	s_nop 1
	v_cndmask_b32_e32 v10, v14, v10, vcc
	v_div_scale_f32 v14, s[0:1], v10, v10, v120
	v_rcp_f32_e32 v16, v14
	v_div_scale_f32 v8, vcc, v120, v10, v120
	v_fma_f32 v6, -v14, v16, 1.0
	v_fmac_f32_e32 v16, v6, v16
	v_pk_add_f32 v[6:7], v[74:75], 0 op_sel_hi:[1,0]
	v_mul_f32_e32 v9, v8, v16
	v_pk_add_f32 v[6:7], v[6:7], v[78:79]
	v_fma_f32 v13, -v14, v9, v8
	v_pk_add_f32 v[6:7], v[6:7], v[80:81]
	v_fmac_f32_e32 v9, v13, v16
	v_pk_add_f32 v[6:7], v[6:7], v[76:77]
	v_fma_f32 v8, -v14, v9, v8
	v_pk_add_f32 v[6:7], v[6:7], v[82:83]
	v_div_fmas_f32 v8, v8, v16, v9
	v_pk_add_f32 v[6:7], v[6:7], v[94:95]
	v_div_fixup_f32 v8, v8, v10, v120
	v_pk_add_f32 v[6:7], v[6:7], v[96:97]
	v_fma_f32 v9, -v11, v8, v121
	v_pk_add_f32 v[6:7], v[6:7], v[84:85]
	s_nop 0
	v_pk_add_f32 v[6:7], v[6:7], v[102:103]
	s_nop 0
	v_pk_add_f32 v[6:7], v[6:7], v[108:109]
	s_nop 0
	v_pk_add_f32 v[6:7], v[6:7], v[110:111]
	s_nop 0
	v_pk_add_f32 v[6:7], v[6:7], v[104:105]
	s_nop 0
	v_pk_add_f32 v[6:7], v[6:7], v[112:113]
	s_nop 0
	v_pk_add_f32 v[6:7], v[6:7], v[116:117]
	s_nop 0
	v_pk_add_f32 v[6:7], v[6:7], v[114:115]
	s_nop 0
	v_pk_add_f32 v[6:7], v[6:7], v[118:119]
	s_nop 0
	v_pk_mul_f32 v[6:7], v[6:7], s[4:5] op_sel_hi:[1,0]
	s_nop 0
	v_fma_f32 v6, -v7, v7, v6
	v_cmp_ngt_f32_e64 s[0:1], 0, v6
	s_nop 1
	v_cndmask_b32_e64 v6, 0, v6, s[0:1]
	v_add_f32_e32 v6, 0x3727c5ac, v6
	v_mul_f32_e32 v12, 0x4f800000, v6
	v_cmp_gt_f32_e64 s[0:1], s5, v6
	s_nop 1
	v_cndmask_b32_e64 v6, v6, v12, s[0:1]
	v_sqrt_f32_e32 v12, v6
	s_nop 0
	v_add_u32_e32 v13, -1, v12
	v_fma_f32 v14, -v13, v12, v6
	v_cmp_ge_f32_e64 s[4:5], 0, v14
	v_add_u32_e32 v14, 1, v12
	s_nop 0
	v_cndmask_b32_e64 v13, v12, v13, s[4:5]
	v_fma_f32 v12, -v14, v12, v6
	v_cmp_lt_f32_e64 s[4:5], 0, v12
	s_nop 1
	v_cndmask_b32_e64 v12, v13, v14, s[4:5]
	v_mul_f32_e32 v13, 0x37800000, v12
	v_cndmask_b32_e64 v12, v12, v13, s[0:1]
	v_cmp_class_f32_e64 s[0:1], v6, v15
	s_cselect_b64 s[4:5], -1, 0
	v_lshlrev_b32_e32 v15, 2, v100
	v_cndmask_b32_e64 v6, v12, v6, s[0:1]
	v_div_scale_f32 v12, s[0:1], v6, v6, v122
	v_rcp_f32_e32 v13, v12
	s_lshl_b64 s[0:1], s[18:19], 2
	s_waitcnt lgkmcnt(0)
	s_add_u32 s0, s14, s0
	s_addc_u32 s1, s15, s1
	v_fma_f32 v10, -v12, v13, 1.0
	v_fmac_f32_e32 v13, v10, v13
	v_div_scale_f32 v10, vcc, v122, v6, v122
	v_mul_f32_e32 v11, v10, v13
	v_fma_f32 v14, -v12, v11, v10
	v_fmac_f32_e32 v11, v14, v13
	v_fma_f32 v10, -v12, v11, v10
	v_div_fmas_f32 v10, v10, v13, v11
	v_div_fixup_f32 v6, v10, v6, v122
	ds_write2st64_b32 v86, v8, v6 offset0:136 offset1:140
	v_fma_f32 v6, -v7, v6, v123
	ds_write2st64_b32 v86, v9, v6 offset0:144 offset1:148
	s_waitcnt lgkmcnt(0)
	s_barrier
	v_and_b32_e32 v14, 7, v0
	ds_read2st64_b32 v[8:9], v15 offset0:136 offset1:144
	v_lshlrev_b32_e32 v6, 5, v14
	v_mov_b32_e32 v7, v87
	v_lshl_add_u64 v[94:95], s[0:1], 0, v[6:7]
	v_cvt_f32_f16_e32 v6, v70
	v_cvt_f32_f16_sdwa v7, v70 dst_sel:DWORD dst_unused:UNUSED_PAD src0_sel:WORD_1
	v_cvt_f32_f16_e32 v12, v71
	v_cvt_f32_f16_sdwa v13, v71 dst_sel:DWORD dst_unused:UNUSED_PAD src0_sel:WORD_1
	s_waitcnt lgkmcnt(0)
	v_mov_b32_e32 v16, v9
	s_cmp_lg_u32 s3, 0
	v_pk_fma_f32 v[10:11], v[8:9], v[6:7], v[16:17] op_sel_hi:[0,1,0]
	v_pk_fma_f32 v[12:13], v[8:9], v[12:13], v[16:17] op_sel_hi:[0,1,0]
	v_pk_fma_f32 v[6:7], v[8:9], v[22:23], v[16:17] op_sel_hi:[0,1,0]
	v_pk_fma_f32 v[8:9], v[8:9], v[24:25], v[16:17] op_sel_hi:[0,1,0]
	s_cmp_lg_u32 s3, 0
	s_cbranch_scc1 .LBB5_2
	v_lshlrev_b32_e32 v16, 14, v100
	v_mov_b32_e32 v17, v87
	v_lshl_add_u64 v[16:17], v[94:95], 0, v[16:17]
	global_store_dwordx4 v[16:17], v[10:13], off nt
	global_store_dwordx4 v[16:17], v[6:9], off offset:16 nt

.LBB5_32:
	s_nop 0
	v_cvt_pk_f16_f32 v38, v38, v39
	v_cvt_pk_f16_f32 v39, v40, v41
	v_cvt_pk_f16_f32 v40, v46, v47
	v_cvt_pk_f16_f32 v41, v48, v49
	ds_write_b128 v106, v[38:41] offset:9216
	s_waitcnt lgkmcnt(0)
	s_barrier
	ds_read_b64_tr_b16 v[38:39], v87 offset:9216
	ds_read_b64_tr_b16 v[40:41], v87 offset:9792
	ds_read_b64_tr_b16 v[48:49], v87 offset:9856
	ds_read_b64_tr_b16 v[46:47], v87 offset:9280
	s_waitcnt vmcnt(3) lgkmcnt(2)
	v_mfma_f32_32x32x16_f16 v[2:17], v[58:61], v[38:41], v[2:17]
	s_lshl_b32 s0, s3, 7
	s_movk_i32 s1, 0x110
	s_lshl_b64 s[4:5], s[16:17], 22
	s_add_u32 s3, s12, s4
	s_addc_u32 s4, s13, s5
	s_lshl_b32 s2, s2, 1
	s_add_u32 s2, s3, s2
	s_waitcnt lgkmcnt(0)
	v_mfma_f32_32x32x16_f16 v[18:33], v[58:61], v[46:49], v[18:33]
	ds_read_b64_tr_b16 v[38:39], v87 offset:11520
	ds_read_b64_tr_b16 v[40:41], v87 offset:12096
	ds_read_b64_tr_b16 v[48:49], v87 offset:12160
	ds_read_b64_tr_b16 v[46:47], v87 offset:11584
	s_addc_u32 s3, s4, 0
	v_lshrrev_b32_e32 v1, 4, v1
	s_waitcnt vmcnt(2) lgkmcnt(2)
	v_mfma_f32_32x32x16_f16 v[2:17], v[54:57], v[38:41], v[2:17]
	s_waitcnt lgkmcnt(0)
	v_mfma_f32_32x32x16_f16 v[18:33], v[54:57], v[46:49], v[18:33]
	ds_read_b64_tr_b16 v[38:39], v87 offset:13824
	ds_read_b64_tr_b16 v[40:41], v87 offset:14400
	ds_read_b64_tr_b16 v[48:49], v87 offset:14464
	ds_read_b64_tr_b16 v[46:47], v87 offset:13888
	s_waitcnt vmcnt(1) lgkmcnt(2)
	v_mfma_f32_32x32x16_f16 v[2:17], v[42:45], v[38:41], v[2:17]
	s_waitcnt lgkmcnt(0)
	v_mfma_f32_32x32x16_f16 v[18:33], v[42:45], v[46:49], v[18:33]
	ds_read_b64_tr_b16 v[38:39], v87 offset:16128
	ds_read_b64_tr_b16 v[40:41], v87 offset:16704
	ds_read_b64_tr_b16 v[44:45], v87 offset:16768
	ds_read_b64_tr_b16 v[42:43], v87 offset:16192
	s_waitcnt lgkmcnt(0)
	s_barrier
	s_waitcnt vmcnt(0)
	v_mfma_f32_32x32x16_f16 v[2:17], v[34:37], v[38:41], v[2:17]
	v_and_b32_e32 v38, 4, v100
	v_lshl_or_b32 v38, v99, 5, v38
	v_and_b32_e32 v39, 31, v0
	v_mul_u32_u24_e32 v38, 0x110, v38
	v_lshl_add_u32 v38, v39, 2, v38
	v_mfma_f32_32x32x16_f16 v[18:33], v[34:37], v[42:45], v[18:33]
	s_nop 11
	ds_write2_b32 v38, v2, v18 offset1:32
	ds_write2_b32 v38, v3, v19 offset0:68 offset1:100
	ds_write2_b32 v38, v4, v20 offset0:136 offset1:168
	ds_write2_b32 v38, v5, v21 offset0:204 offset1:236
	v_add_u32_e32 v2, 0x800, v38
	ds_write2_b32 v2, v6, v22 offset0:32 offset1:64
	ds_write2_b32 v2, v7, v23 offset0:100 offset1:132
	ds_write2_b32 v2, v8, v24 offset0:168 offset1:200
	v_add_u32_e32 v2, 0xa00, v38
	ds_write2_b32 v2, v9, v25 offset0:108 offset1:140
	v_add_u32_e32 v2, 0x1000, v38
	ds_write2_b32 v2, v10, v26 offset0:64 offset1:96
	ds_write2_b32 v2, v11, v27 offset0:132 offset1:164
	ds_write2_b32 v2, v12, v28 offset0:200 offset1:232
	v_add_u32_e32 v2, 0x1400, v38
	ds_write2_b32 v2, v13, v29 offset0:12 offset1:44
	v_add_u32_e32 v2, 0x1800, v38
	ds_write2_b32 v2, v14, v30 offset0:96 offset1:128
	ds_write2_b32 v2, v15, v31 offset0:164 offset1:196
	v_add_u32_e32 v2, 0x1a00, v38
	ds_write2_b32 v2, v16, v32 offset0:104 offset1:136
	v_add_u32_e32 v2, 0x1c00, v38
	v_lshrrev_b32_e32 v6, 4, v0
	ds_write2_b32 v2, v17, v33 offset0:44 offset1:76
	v_or_b32_e32 v2, s0, v6
	v_ashrrev_i32_e32 v3, 31, v2
	v_lshl_add_u64 v[4:5], v[2:3], 2, s[10:11]
	s_waitcnt lgkmcnt(0)
	s_barrier
	v_and_b32_e32 v4, 15, v0
	v_lshlrev_b32_e32 v18, 4, v4
	v_lshlrev_b32_e32 v10, 3, v4
	v_mad_u32_u24 v4, v6, s1, v18
	ds_read_b128 v[60:63], v4
	ds_read_b128 v[64:67], v4 offset:4352
	ds_read_b128 v[68:71], v4 offset:8704
	ds_read_b128 v[72:75], v4 offset:13056
	ds_read_b128 v[76:79], v4 offset:17408
	ds_read_b128 v[80:83], v4 offset:21760
	ds_read_b128 v[84:87], v4 offset:26112
	ds_read_b128 v[88:91], v4 offset:30464
	v_mov_b32_e32 v11, 0
	v_lshlrev_b64 v[14:15], 13, v[2:3]
	v_lshl_add_u64 v[12:13], s[2:3], 0, v[10:11]
	v_lshl_add_u64 v[12:13], v[12:13], 0, v[14:15]
	s_mov_b32 s4, 0x20000
	s_mov_b32 s5, 0
	s_waitcnt lgkmcnt(7)
	v_pk_add_f32 v[60:61], v[60:61], v[124:125] op_sel_hi:[1,0]
	v_pk_add_f32 v[62:63], v[62:63], v[124:125] op_sel_hi:[1,0]
	v_cvt_pk_f16_f32 v60, v60, v61
	v_cvt_pk_f16_f32 v61, v62, v63
	global_store_dwordx2 v[12:13], v[60:61], off
	v_lshl_add_u64 v[12:13], v[12:13], 0, s[4:5]
	s_waitcnt lgkmcnt(6)
	v_pk_add_f32 v[64:65], v[64:65], v[126:127] op_sel_hi:[1,0]
	v_pk_add_f32 v[66:67], v[66:67], v[126:127] op_sel_hi:[1,0]
	v_cvt_pk_f16_f32 v64, v64, v65
	v_cvt_pk_f16_f32 v65, v66, v67
	global_store_dwordx2 v[12:13], v[64:65], off
	v_lshl_add_u64 v[12:13], v[12:13], 0, s[4:5]
	s_waitcnt lgkmcnt(5)
	v_pk_add_f32 v[68:69], v[68:69], v[128:129] op_sel_hi:[1,0]
	v_pk_add_f32 v[70:71], v[70:71], v[128:129] op_sel_hi:[1,0]
	v_cvt_pk_f16_f32 v68, v68, v69
	v_cvt_pk_f16_f32 v69, v70, v71
	global_store_dwordx2 v[12:13], v[68:69], off
	v_lshl_add_u64 v[12:13], v[12:13], 0, s[4:5]
	s_waitcnt lgkmcnt(4)
	v_pk_add_f32 v[72:73], v[72:73], v[130:131] op_sel_hi:[1,0]
	v_pk_add_f32 v[74:75], v[74:75], v[130:131] op_sel_hi:[1,0]
	v_cvt_pk_f16_f32 v72, v72, v73
	v_cvt_pk_f16_f32 v73, v74, v75
	global_store_dwordx2 v[12:13], v[72:73], off
	v_lshl_add_u64 v[12:13], v[12:13], 0, s[4:5]
	s_waitcnt lgkmcnt(3)
	v_pk_add_f32 v[76:77], v[76:77], v[132:133] op_sel_hi:[1,0]
	v_pk_add_f32 v[78:79], v[78:79], v[132:133] op_sel_hi:[1,0]
	v_cvt_pk_f16_f32 v76, v76, v77
	v_cvt_pk_f16_f32 v77, v78, v79
	global_store_dwordx2 v[12:13], v[76:77], off
	v_lshl_add_u64 v[12:13], v[12:13], 0, s[4:5]
	s_waitcnt lgkmcnt(2)
	v_pk_add_f32 v[80:81], v[80:81], v[134:135] op_sel_hi:[1,0]
	v_pk_add_f32 v[82:83], v[82:83], v[134:135] op_sel_hi:[1,0]
	v_cvt_pk_f16_f32 v80, v80, v81
	v_cvt_pk_f16_f32 v81, v82, v83
	global_store_dwordx2 v[12:13], v[80:81], off
	v_lshl_add_u64 v[12:13], v[12:13], 0, s[4:5]
	s_waitcnt lgkmcnt(1)
	v_pk_add_f32 v[84:85], v[84:85], v[136:137] op_sel_hi:[1,0]
	v_pk_add_f32 v[86:87], v[86:87], v[136:137] op_sel_hi:[1,0]
	v_cvt_pk_f16_f32 v84, v84, v85
	v_cvt_pk_f16_f32 v85, v86, v87
	global_store_dwordx2 v[12:13], v[84:85], off
	v_lshl_add_u64 v[12:13], v[12:13], 0, s[4:5]
	s_waitcnt lgkmcnt(0)
	v_pk_add_f32 v[88:89], v[88:89], v[138:139] op_sel_hi:[1,0]
	v_pk_add_f32 v[90:91], v[90:91], v[138:139] op_sel_hi:[1,0]
	v_cvt_pk_f16_f32 v88, v88, v89
	v_cvt_pk_f16_f32 v89, v90, v91
	global_store_dwordx2 v[12:13], v[88:89], off
	s_endpgm
	.p2alignl 8, 3212836864

	.amdhsa_kernel _Z9k_gemm_tlILi2ELb1EEvPKDF16_6TlArgs
		.amdhsa_group_segment_fixed_size 38912
		.amdhsa_private_segment_fixed_size 0
		.amdhsa_kernarg_size 80
		.amdhsa_user_sgpr_count 2
		.amdhsa_user_sgpr_dispatch_ptr 0
		.amdhsa_user_sgpr_queue_ptr 0
		.amdhsa_user_sgpr_kernarg_segment_ptr 1
		.amdhsa_user_sgpr_dispatch_id 0
		.amdhsa_user_sgpr_kernarg_preload_length 0
		.amdhsa_user_sgpr_kernarg_preload_offset 0
		.amdhsa_user_sgpr_private_segment_size 0
		.amdhsa_uses_dynamic_stack 0
		.amdhsa_enable_private_segment 0
		.amdhsa_system_sgpr_workgroup_id_x 1
		.amdhsa_system_sgpr_workgroup_id_y 1
		.amdhsa_system_sgpr_workgroup_id_z 0
		.amdhsa_system_sgpr_workgroup_info 0
		.amdhsa_system_vgpr_workitem_id 0
		.amdhsa_next_free_vgpr 169
		.amdhsa_next_free_sgpr 96
		.amdhsa_accum_offset 144
		.amdhsa_reserve_vcc 1
		.amdhsa_float_round_mode_32 0
		.amdhsa_float_round_mode_16_64 0
		.amdhsa_float_denorm_mode_32 3
		.amdhsa_float_denorm_mode_16_64 3
		.amdhsa_dx10_clamp 1
		.amdhsa_ieee_mode 1
		.amdhsa_fp16_overflow 0
		.amdhsa_tg_split 0
		.amdhsa_exception_fp_ieee_invalid_op 0
		.amdhsa_exception_fp_denorm_src 0
		.amdhsa_exception_fp_ieee_div_zero 0
		.amdhsa_exception_fp_ieee_overflow 0
		.amdhsa_exception_fp_ieee_underflow 0
		.amdhsa_exception_fp_ieee_inexact 0
		.amdhsa_exception_int_div_zero 0
	.end_amdhsa_kernel

amdhsa.kernels:
  - .agpr_count:     0
    .args:
      - .actual_access:  read_only
        .address_space:  global
        .offset:         0
        .size:           8
        .value_kind:     global_buffer
      - .actual_access:  read_only
        .address_space:  global
        .offset:         8
        .size:           8
        .value_kind:     global_buffer
      - .actual_access:  read_only
        .address_space:  global
        .offset:         16
        .size:           8
        .value_kind:     global_buffer
      - .actual_access:  write_only
        .address_space:  global
        .offset:         24
        .size:           8
        .value_kind:     global_buffer
      - .actual_access:  write_only
        .address_space:  global
        .offset:         32
        .size:           8
        .value_kind:     global_buffer
      - .actual_access:  write_only
        .address_space:  global
        .offset:         40
        .size:           8
        .value_kind:     global_buffer
      - .offset:         48
        .size:           104
        .value_kind:     by_value
    .group_segment_fixed_size: 37248
    .kernarg_segment_align: 8
    .kernarg_segment_size: 152
    .language:       OpenCL C
    .language_version:
      - 2
      - 0
    .max_flat_workgroup_size: 512
    .name:           _Z4k_lnPKfS0_S0_PDF16_PfS2_7CvtArgs
    .private_segment_fixed_size: 0
    .sgpr_count:     40
    .sgpr_spill_count: 0
    .symbol:         _Z4k_lnPKfS0_S0_PDF16_PfS2_7CvtArgs.kd
    .uniform_work_group_size: 1
    .uses_dynamic_stack: false
    .vgpr_count:     118
    .vgpr_spill_count: 0
    .wavefront_size: 64
  - .agpr_count:     36
    .args:
      - .actual_access:  read_only
        .address_space:  global
        .offset:         0
        .size:           8
        .value_kind:     global_buffer
      - .actual_access:  read_only
        .address_space:  global
        .offset:         8
        .size:           8
        .value_kind:     global_buffer
      - .actual_access:  read_only
        .address_space:  global
        .offset:         16
        .size:           8
        .value_kind:     global_buffer
      - .actual_access:  read_only
        .address_space:  global
        .offset:         24
        .size:           8
        .value_kind:     global_buffer
      - .actual_access:  read_only
        .address_space:  global
        .offset:         32
        .size:           8
        .value_kind:     global_buffer
      - .actual_access:  read_only
        .address_space:  global
        .offset:         40
        .size:           8
        .value_kind:     global_buffer
      - .actual_access:  read_only
        .address_space:  global
        .offset:         48
        .size:           8
        .value_kind:     global_buffer
      - .actual_access:  read_only
        .address_space:  global
        .offset:         56
        .size:           8
        .value_kind:     global_buffer
      - .actual_access:  write_only
        .address_space:  global
        .offset:         64
        .size:           8
        .value_kind:     global_buffer
      - .actual_access:  write_only
        .address_space:  global
        .offset:         72
        .size:           8
        .value_kind:     global_buffer
      - .actual_access:  write_only
        .address_space:  global
        .offset:         80
        .size:           8
        .value_kind:     global_buffer
      - .actual_access:  write_only
        .address_space:  global
        .offset:         88
        .size:           8
        .value_kind:     global_buffer
      - .actual_access:  write_only
        .address_space:  global
        .offset:         96
        .size:           8
        .value_kind:     global_buffer
    .group_segment_fixed_size: 77312
    .kernarg_segment_align: 8
    .kernarg_segment_size: 104
    .language:       OpenCL C
    .language_version:
      - 2
      - 0
    .max_flat_workgroup_size: 256
    .name:           _Z7k_frontPKDF16_S0_PKfS2_S0_S2_S2_S2_PjPfS4_S4_S4_
    .private_segment_fixed_size: 0
    .sgpr_count:     25
    .sgpr_spill_count: 0
    .symbol:         _Z7k_frontPKDF16_S0_PKfS2_S0_S2_S2_S2_PjPfS4_S4_S4_.kd
    .uniform_work_group_size: 1
    .uses_dynamic_stack: false
    .vgpr_count:     204
    .vgpr_spill_count: 0
    .wavefront_size: 64
  - .agpr_count:     0
    .args:
      - .actual_access:  read_only
        .address_space:  global
        .offset:         0
        .size:           8
        .value_kind:     global_buffer
      - .address_space:  global
        .offset:         8
        .size:           8
        .value_kind:     global_buffer
      - .actual_access:  read_only
        .address_space:  global
        .offset:         16
        .size:           8
        .value_kind:     global_buffer
    .group_segment_fixed_size: 0
    .kernarg_segment_align: 8
    .kernarg_segment_size: 24
    .language:       OpenCL C
    .language_version:
      - 2
      - 0
    .max_flat_workgroup_size: 64
    .name:           _Z7k_scan2PKfPfS0_
    .private_segment_fixed_size: 0
    .sgpr_count:     48
    .sgpr_spill_count: 0
    .symbol:         _Z7k_scan2PKfPfS0_.kd
    .uniform_work_group_size: 1
    .uses_dynamic_stack: false
    .vgpr_count:     150
    .vgpr_spill_count: 0
    .wavefront_size: 64
  - .agpr_count:     0
    .args:
      - .actual_access:  read_only
        .address_space:  global
        .offset:         0
        .size:           8
        .value_kind:     global_buffer
      - .actual_access:  read_only
        .address_space:  global
        .offset:         8
        .size:           8
        .value_kind:     global_buffer
      - .actual_access:  read_only
        .address_space:  global
        .offset:         16
        .size:           8
        .value_kind:     global_buffer
      - .actual_access:  read_only
        .address_space:  global
        .offset:         24
        .size:           8
        .value_kind:     global_buffer
      - .actual_access:  read_only
        .address_space:  global
        .offset:         32
        .size:           8
        .value_kind:     global_buffer
      - .actual_access:  read_only
        .address_space:  global
        .offset:         40
        .size:           8
        .value_kind:     global_buffer
      - .actual_access:  read_only
        .address_space:  global
        .offset:         48
        .size:           8
        .value_kind:     global_buffer
      - .actual_access:  read_only
        .address_space:  global
        .offset:         56
        .size:           8
        .value_kind:     global_buffer
      - .actual_access:  read_only
        .address_space:  global
        .offset:         64
        .size:           8
        .value_kind:     global_buffer
      - .offset:         72
        .size:           72
        .value_kind:     by_value
    .group_segment_fixed_size: 60416
    .kernarg_segment_align: 8
    .kernarg_segment_size: 144
    .language:       OpenCL C
    .language_version:
      - 2
      - 0
    .max_flat_workgroup_size: 256
    .name:           _Z7k_scan3PKjPKfS2_S2_S2_S2_PKDF16_S4_S4_7EpiArgs
    .private_segment_fixed_size: 0
    .sgpr_count:     34
    .sgpr_spill_count: 0
    .symbol:         _Z7k_scan3PKjPKfS2_S2_S2_S2_PKDF16_S4_S4_7EpiArgs.kd
    .uniform_work_group_size: 1
    .uses_dynamic_stack: false
    .vgpr_count:     236
    .vgpr_spill_count: 0
    .wavefront_size: 64
  - .agpr_count:     0
    .args:
      - .actual_access:  read_only
        .address_space:  global
        .offset:         0
        .size:           8
        .value_kind:     global_buffer
      - .actual_access:  read_only
        .address_space:  global
        .offset:         8
        .size:           8
        .value_kind:     global_buffer
      - .actual_access:  read_only
        .address_space:  global
        .offset:         16
        .size:           8
        .value_kind:     global_buffer
      - .actual_access:  write_only
        .address_space:  global
        .offset:         24
        .size:           8
        .value_kind:     global_buffer
    .group_segment_fixed_size: 20160
    .kernarg_segment_align: 8
    .kernarg_segment_size: 32
    .language:       OpenCL C
    .language_version:
      - 2
      - 0
    .max_flat_workgroup_size: 256
    .name:           _Z8k_dwconvPKDF16_PKfS2_PDF16_
    .private_segment_fixed_size: 0
    .sgpr_count:     86
    .sgpr_spill_count: 0
    .symbol:         _Z8k_dwconvPKDF16_PKfS2_PDF16_.kd
    .uniform_work_group_size: 1
    .uses_dynamic_stack: false
    .vgpr_count:     65
    .vgpr_spill_count: 0
    .wavefront_size: 64
  - .agpr_count:     0
    .args:
      - .actual_access:  read_only
        .address_space:  global
        .offset:         0
        .size:           8
        .value_kind:     global_buffer
      - .offset:         8
        .size:           72
        .value_kind:     by_value
    .group_segment_fixed_size: 38912
    .kernarg_segment_align: 8
    .kernarg_segment_size: 80
    .language:       OpenCL C
    .language_version:
      - 2
      - 0
    .max_flat_workgroup_size: 256
    .name:           _Z9k_gemm_tlILi2ELb1EEvPKDF16_6TlArgs
    .private_segment_fixed_size: 0
    .sgpr_count:     27
    .sgpr_spill_count: 0
    .symbol:         _Z9k_gemm_tlILi2ELb1EEvPKDF16_6TlArgs.kd
    .uniform_work_group_size: 1
    .uses_dynamic_stack: false
    .vgpr_count:     141
    .vgpr_spill_count: 0
    .wavefront_size: 64
  - .agpr_count:     0
    .args:
      - .actual_access:  read_only
        .address_space:  global
        .offset:         0
        .size:           8
        .value_kind:     global_buffer
      - .offset:         8
        .size:           72
        .value_kind:     by_value
    .group_segment_fixed_size: 34816
    .kernarg_segment_align: 8
    .kernarg_segment_size: 80
    .language:       OpenCL C
    .language_version:
      - 2
      - 0
    .max_flat_workgroup_size: 256
    .name:           _Z9k_gemm_tlILi3ELb0EEvPKDF16_6TlArgs
    .private_segment_fixed_size: 0
    .sgpr_count:     18
    .sgpr_spill_count: 0
    .symbol:         _Z9k_gemm_tlILi3ELb0EEvPKDF16_6TlArgs.kd
    .uniform_work_group_size: 1
    .uses_dynamic_stack: false
    .vgpr_count:     127
    .vgpr_spill_count: 0
    .wavefront_size: 64
